# baseline (speedup 1.0000x reference)
.LBB1_6:
	s_mul_i32 s18, s33, 0xc0
	s_barrier
	v_and_b32_e32 v110, 15, v0
	v_bfe_u32 v111, v0, 4, 2
	s_lshl_b32 s52, s40, 5
	v_or_b32_e32 v112, s52, v110
	v_mul_u32_u24_e32 v113, 0x90, v112
	v_lshl_add_u32 v113, v111, 3, v113
	v_bfe_u32 v114, v0, 2, 1
	v_bfe_u32 v115, v0, 3, 1
	v_lshlrev_b32_e32 v114, 3, v114
	v_lshl_or_b32 v114, v115, 2, v114
	v_and_b32_e32 v115, 3, v0
	v_or_b32_e32 v114, v114, v115
	v_or_b32_e32 v114, s52, v114
	v_lshlrev_b32_e32 v114, 1, v114
	v_mul_u32_u24_e32 v115, 0x840, v111
	v_add_u32_e32 v114, v114, v115
	v_mov_b32_e32 v116, 0x3e38aa3b
	v_mov_b32_e32 v117, 0x3e38aa3b
	v_lshrrev_b32_e32 v128, 3, v0
	v_mul_u32_u24_e32 v128, 0x90, v128
	v_and_b32_e32 v129, 7, v0
	v_lshl_add_u32 v128, v129, 4, v128
	v_lshrrev_b32_e32 v130, 5, v0
	v_mul_u32_u24_e32 v129, 0x210, v130
	v_and_b32_e32 v131, 31, v0
	v_lshl_add_u32 v129, v131, 4, v129
	v_lshlrev_b32_e32 v130, 12, v130
	v_lshl_add_u32 v130, v131, 4, v130
	s_cmp_lg_u32 s37, 0
	s_cbranch_scc1 .Lmy_st0_wr1
	s_add_i32 s54, s18, 0
	s_lshr_b32 s55, s54, 10
	v_pk_add_f32 v[98:99], v[188:189], v[98:99]
	v_pk_add_f32 v[100:101], v[190:191], v[100:101]
	v_pk_add_f32 v[90:91], v[188:189], v[90:91]
	v_pk_add_f32 v[92:93], v[190:191], v[92:93]
	v_pk_add_f32 v[86:87], v[188:189], v[86:87]
	v_pk_add_f32 v[88:89], v[190:191], v[88:89]
	v_pk_add_f32 v[82:83], v[188:189], v[82:83]
	v_pk_add_f32 v[84:85], v[190:191], v[84:85]
	s_cmp_eq_u32 s55, 2
	s_cbranch_scc1 .Lmy_s1_v
	v_add_u32_e32 v118, 0x0, v113
	s_cmp_eq_u32 s55, 0
	s_cbranch_scc0 .Lmy_s1_ns
	v_pk_mul_f32 v[98:99], v[116:117], v[98:99]
	v_pk_mul_f32 v[100:101], v[116:117], v[100:101]
	v_pk_mul_f32 v[90:91], v[116:117], v[90:91]
	v_pk_mul_f32 v[92:93], v[116:117], v[92:93]
	v_pk_mul_f32 v[86:87], v[116:117], v[86:87]
	v_pk_mul_f32 v[88:89], v[116:117], v[88:89]
	v_pk_mul_f32 v[82:83], v[116:117], v[82:83]
	v_pk_mul_f32 v[84:85], v[116:117], v[84:85]

.Lmy_s1_v:
	v_add_u32_e32 v118, 0x0, v114
	v_cvt_pk_f16_f32 v120, v98, v99
	v_cvt_pk_f16_f32 v121, v100, v101
	v_cvt_pk_f16_f32 v122, v90, v91
	v_cvt_pk_f16_f32 v123, v92, v93
	v_cvt_pk_f16_f32 v124, v86, v87
	v_cvt_pk_f16_f32 v125, v88, v89
	v_cvt_pk_f16_f32 v126, v82, v83
	v_cvt_pk_f16_f32 v127, v84, v85
	ds_write_b16 v118, v120
	ds_write_b16_d16_hi v118, v120 offset:528
	ds_write_b16 v118, v121 offset:1056
	ds_write_b16_d16_hi v118, v121 offset:1584
	ds_write_b16 v118, v122 offset:32
	ds_write_b16_d16_hi v118, v122 offset:560
	ds_write_b16 v118, v123 offset:1088
	ds_write_b16_d16_hi v118, v123 offset:1616
	ds_write_b16 v118, v124 offset:256
	ds_write_b16_d16_hi v118, v124 offset:784
	ds_write_b16 v118, v125 offset:1312
	ds_write_b16_d16_hi v118, v125 offset:1840
	ds_write_b16 v118, v126 offset:288
	ds_write_b16_d16_hi v118, v126 offset:816
	ds_write_b16 v118, v127 offset:1344
	ds_write_b16_d16_hi v118, v127 offset:1872
.Lmy_s1_end:
	s_add_i32 s54, s18, 16
	s_lshr_b32 s55, s54, 10
	v_pk_add_f32 v[78:79], v[192:193], v[78:79]
	v_pk_add_f32 v[80:81], v[194:195], v[80:81]
	v_pk_add_f32 v[74:75], v[192:193], v[74:75]
	v_pk_add_f32 v[76:77], v[194:195], v[76:77]
	v_pk_add_f32 v[70:71], v[192:193], v[70:71]
	v_pk_add_f32 v[72:73], v[194:195], v[72:73]
	v_pk_add_f32 v[66:67], v[192:193], v[66:67]
	v_pk_add_f32 v[68:69], v[194:195], v[68:69]
	s_cmp_eq_u32 s55, 2
	s_cbranch_scc1 .Lmy_s2_v
	v_add_u32_e32 v118, 0x20, v113
	s_cmp_eq_u32 s55, 0
	s_cbranch_scc0 .Lmy_s2_ns
	v_pk_mul_f32 v[78:79], v[116:117], v[78:79]
	v_pk_mul_f32 v[80:81], v[116:117], v[80:81]
	v_pk_mul_f32 v[74:75], v[116:117], v[74:75]
	v_pk_mul_f32 v[76:77], v[116:117], v[76:77]
	v_pk_mul_f32 v[70:71], v[116:117], v[70:71]
	v_pk_mul_f32 v[72:73], v[116:117], v[72:73]
	v_pk_mul_f32 v[66:67], v[116:117], v[66:67]
	v_pk_mul_f32 v[68:69], v[116:117], v[68:69]

.Lmy_s2_v:
	v_add_u32_e32 v118, 0x2100, v114
	v_cvt_pk_f16_f32 v120, v78, v79
	v_cvt_pk_f16_f32 v121, v80, v81
	v_cvt_pk_f16_f32 v122, v74, v75
	v_cvt_pk_f16_f32 v123, v76, v77
	v_cvt_pk_f16_f32 v124, v70, v71
	v_cvt_pk_f16_f32 v125, v72, v73
	v_cvt_pk_f16_f32 v126, v66, v67
	v_cvt_pk_f16_f32 v127, v68, v69
	ds_write_b16 v118, v120
	ds_write_b16_d16_hi v118, v120 offset:528
	ds_write_b16 v118, v121 offset:1056
	ds_write_b16_d16_hi v118, v121 offset:1584
	ds_write_b16 v118, v122 offset:32
	ds_write_b16_d16_hi v118, v122 offset:560
	ds_write_b16 v118, v123 offset:1088
	ds_write_b16_d16_hi v118, v123 offset:1616
	ds_write_b16 v118, v124 offset:256
	ds_write_b16_d16_hi v118, v124 offset:784
	ds_write_b16 v118, v125 offset:1312
	ds_write_b16_d16_hi v118, v125 offset:1840
	ds_write_b16 v118, v126 offset:288
	ds_write_b16_d16_hi v118, v126 offset:816
	ds_write_b16 v118, v127 offset:1344
	ds_write_b16_d16_hi v118, v127 offset:1872
.Lmy_s2_end:
	s_add_i32 s54, s18, 32
	s_lshr_b32 s55, s54, 10
	v_pk_add_f32 v[62:63], v[196:197], v[62:63]
	v_pk_add_f32 v[64:65], v[198:199], v[64:65]
	v_pk_add_f32 v[58:59], v[196:197], v[58:59]
	v_pk_add_f32 v[60:61], v[198:199], v[60:61]
	v_pk_add_f32 v[54:55], v[196:197], v[54:55]
	v_pk_add_f32 v[56:57], v[198:199], v[56:57]
	v_pk_add_f32 v[50:51], v[196:197], v[50:51]
	v_pk_add_f32 v[52:53], v[198:199], v[52:53]
	s_cmp_eq_u32 s55, 2
	s_cbranch_scc1 .Lmy_s3_v
	v_add_u32_e32 v118, 0x40, v113
	s_cmp_eq_u32 s55, 0
	s_cbranch_scc0 .Lmy_s3_ns
	v_pk_mul_f32 v[62:63], v[116:117], v[62:63]
	v_pk_mul_f32 v[64:65], v[116:117], v[64:65]
	v_pk_mul_f32 v[58:59], v[116:117], v[58:59]
	v_pk_mul_f32 v[60:61], v[116:117], v[60:61]
	v_pk_mul_f32 v[54:55], v[116:117], v[54:55]
	v_pk_mul_f32 v[56:57], v[116:117], v[56:57]
	v_pk_mul_f32 v[50:51], v[116:117], v[50:51]
	v_pk_mul_f32 v[52:53], v[116:117], v[52:53]

.Lmy_s3_v:
	v_add_u32_e32 v118, 0x4200, v114
	v_cvt_pk_f16_f32 v120, v62, v63
	v_cvt_pk_f16_f32 v121, v64, v65
	v_cvt_pk_f16_f32 v122, v58, v59
	v_cvt_pk_f16_f32 v123, v60, v61
	v_cvt_pk_f16_f32 v124, v54, v55
	v_cvt_pk_f16_f32 v125, v56, v57
	v_cvt_pk_f16_f32 v126, v50, v51
	v_cvt_pk_f16_f32 v127, v52, v53
	ds_write_b16 v118, v120
	ds_write_b16_d16_hi v118, v120 offset:528
	ds_write_b16 v118, v121 offset:1056
	ds_write_b16_d16_hi v118, v121 offset:1584
	ds_write_b16 v118, v122 offset:32
	ds_write_b16_d16_hi v118, v122 offset:560
	ds_write_b16 v118, v123 offset:1088
	ds_write_b16_d16_hi v118, v123 offset:1616
	ds_write_b16 v118, v124 offset:256
	ds_write_b16_d16_hi v118, v124 offset:784
	ds_write_b16 v118, v125 offset:1312
	ds_write_b16_d16_hi v118, v125 offset:1840
	ds_write_b16 v118, v126 offset:288
	ds_write_b16_d16_hi v118, v126 offset:816
	ds_write_b16 v118, v127 offset:1344
	ds_write_b16_d16_hi v118, v127 offset:1872
.Lmy_s3_end:
	s_branch .Lmy_st0_done
.Lmy_st0_wr1:
	s_add_i32 s54, s18, 48
	s_lshr_b32 s55, s54, 10
	v_pk_add_f32 v[98:99], v[188:189], v[98:99]
	v_pk_add_f32 v[100:101], v[190:191], v[100:101]
	v_pk_add_f32 v[90:91], v[188:189], v[90:91]
	v_pk_add_f32 v[92:93], v[190:191], v[92:93]
	v_pk_add_f32 v[86:87], v[188:189], v[86:87]
	v_pk_add_f32 v[88:89], v[190:191], v[88:89]
	v_pk_add_f32 v[82:83], v[188:189], v[82:83]
	v_pk_add_f32 v[84:85], v[190:191], v[84:85]
	s_cmp_eq_u32 s55, 2
	s_cbranch_scc1 .Lmy_s4_v
	v_add_u32_e32 v118, 0x60, v113
	s_cmp_eq_u32 s55, 0
	s_cbranch_scc0 .Lmy_s4_ns
	v_pk_mul_f32 v[98:99], v[116:117], v[98:99]
	v_pk_mul_f32 v[100:101], v[116:117], v[100:101]
	v_pk_mul_f32 v[90:91], v[116:117], v[90:91]
	v_pk_mul_f32 v[92:93], v[116:117], v[92:93]
	v_pk_mul_f32 v[86:87], v[116:117], v[86:87]
	v_pk_mul_f32 v[88:89], v[116:117], v[88:89]
	v_pk_mul_f32 v[82:83], v[116:117], v[82:83]
	v_pk_mul_f32 v[84:85], v[116:117], v[84:85]

.Lmy_s4_v:
	v_add_u32_e32 v118, 0x6300, v114
	v_cvt_pk_f16_f32 v120, v98, v99
	v_cvt_pk_f16_f32 v121, v100, v101
	v_cvt_pk_f16_f32 v122, v90, v91
	v_cvt_pk_f16_f32 v123, v92, v93
	v_cvt_pk_f16_f32 v124, v86, v87
	v_cvt_pk_f16_f32 v125, v88, v89
	v_cvt_pk_f16_f32 v126, v82, v83
	v_cvt_pk_f16_f32 v127, v84, v85
	ds_write_b16 v118, v120
	ds_write_b16_d16_hi v118, v120 offset:528
	ds_write_b16 v118, v121 offset:1056
	ds_write_b16_d16_hi v118, v121 offset:1584
	ds_write_b16 v118, v122 offset:32
	ds_write_b16_d16_hi v118, v122 offset:560
	ds_write_b16 v118, v123 offset:1088
	ds_write_b16_d16_hi v118, v123 offset:1616
	ds_write_b16 v118, v124 offset:256
	ds_write_b16_d16_hi v118, v124 offset:784
	ds_write_b16 v118, v125 offset:1312
	ds_write_b16_d16_hi v118, v125 offset:1840
	ds_write_b16 v118, v126 offset:288
	ds_write_b16_d16_hi v118, v126 offset:816
	ds_write_b16 v118, v127 offset:1344
	ds_write_b16_d16_hi v118, v127 offset:1872
.Lmy_s4_end:
.Lmy_st0_done:
	s_waitcnt lgkmcnt(0)
	s_barrier
	s_add_i32 s54, s18, 0
	s_lshr_b32 s55, s54, 10
	s_bfe_u32 s56, s54, 0x40006
	s_lshr_b32 s57, s36, 3
	s_lshl_b32 s57, s57, 4
	s_add_i32 s57, s57, s56
	s_lshl_b32 s57, s57, 18
	s_and_b32 s58, s36, 7
	s_cmp_eq_u32 s55, 2
	s_cbranch_scc1 .Lmy_gs0_v
	s_lshl_b32 s58, s58, 15
	s_add_i32 s57, s57, s58
	s_cmp_eq_u32 s55, 0
	s_cselect_b32 s60, s6, s8
	s_cselect_b32 s61, s7, s9
	s_add_u32 s60, s60, s57
	s_addc_u32 s61, s61, 0
	v_mov_b32_e32 v131, v128
	ds_read_b128 v[132:135], v131
	ds_read_b128 v[136:139], v131 offset:9216
	ds_read_b128 v[140:143], v131 offset:18432
	ds_read_b128 v[144:147], v131 offset:27648
	s_waitcnt lgkmcnt(3)
	global_store_dwordx4 v1, v[132:135], s[60:61] nt
	s_add_u32 s60, s60, 0x2000
	s_addc_u32 s61, s61, 0
	s_waitcnt lgkmcnt(2)
	global_store_dwordx4 v1, v[136:139], s[60:61] nt
	s_add_u32 s60, s60, 0x2000
	s_addc_u32 s61, s61, 0
	s_waitcnt lgkmcnt(1)
	global_store_dwordx4 v1, v[140:143], s[60:61] nt
	s_add_u32 s60, s60, 0x2000
	s_addc_u32 s61, s61, 0
	s_waitcnt lgkmcnt(0)
	global_store_dwordx4 v1, v[144:147], s[60:61] nt
	s_branch .Lmy_gs0_end
.Lmy_gs0_v:
	s_lshl_b32 s58, s58, 9
	s_add_i32 s57, s57, s58
	s_add_u32 s60, s10, s57
	s_addc_u32 s61, s11, 0
	v_mov_b32_e32 v131, v129
	ds_read_b128 v[132:135], v131
	ds_read_b128 v[136:139], v131 offset:8448
	ds_read_b128 v[140:143], v131 offset:16896
	ds_read_b128 v[144:147], v131 offset:25344
	s_waitcnt lgkmcnt(3)
	global_store_dwordx4 v130, v[132:135], s[60:61] nt
	s_add_u32 s60, s60, 0x10000
	s_addc_u32 s61, s61, 0
	s_waitcnt lgkmcnt(2)
	global_store_dwordx4 v130, v[136:139], s[60:61] nt
	s_add_u32 s60, s60, 0x10000
	s_addc_u32 s61, s61, 0
	s_waitcnt lgkmcnt(1)
	global_store_dwordx4 v130, v[140:143], s[60:61] nt
	s_add_u32 s60, s60, 0x10000
	s_addc_u32 s61, s61, 0
	s_waitcnt lgkmcnt(0)
	global_store_dwordx4 v130, v[144:147], s[60:61] nt
.Lmy_gs0_end:
	s_cmp_lg_u32 s37, 0
	s_cbranch_scc1 .Lmy_st1_wr1
	s_add_i32 s54, s18, 96
	s_lshr_b32 s55, s54, 10
	v_pk_add_f32 v[46:47], v[200:201], v[46:47]
	v_pk_add_f32 v[48:49], v[202:203], v[48:49]
	v_pk_add_f32 v[42:43], v[200:201], v[42:43]
	v_pk_add_f32 v[44:45], v[202:203], v[44:45]
	v_pk_add_f32 v[38:39], v[200:201], v[38:39]
	v_pk_add_f32 v[40:41], v[202:203], v[40:41]
	v_pk_add_f32 v[34:35], v[200:201], v[34:35]
	v_pk_add_f32 v[36:37], v[202:203], v[36:37]
	s_cmp_eq_u32 s55, 2
	s_cbranch_scc1 .Lmy_s5_v
	v_add_u32_e32 v118, 0x9040, v113
	s_cmp_eq_u32 s55, 0
	s_cbranch_scc0 .Lmy_s5_ns
	v_pk_mul_f32 v[46:47], v[116:117], v[46:47]
	v_pk_mul_f32 v[48:49], v[116:117], v[48:49]
	v_pk_mul_f32 v[42:43], v[116:117], v[42:43]
	v_pk_mul_f32 v[44:45], v[116:117], v[44:45]
	v_pk_mul_f32 v[38:39], v[116:117], v[38:39]
	v_pk_mul_f32 v[40:41], v[116:117], v[40:41]
	v_pk_mul_f32 v[34:35], v[116:117], v[34:35]
	v_pk_mul_f32 v[36:37], v[116:117], v[36:37]

.Lmy_s5_v:
	v_add_u32_e32 v118, 0xd200, v114
	v_cvt_pk_f16_f32 v120, v46, v47
	v_cvt_pk_f16_f32 v121, v48, v49
	v_cvt_pk_f16_f32 v122, v42, v43
	v_cvt_pk_f16_f32 v123, v44, v45
	v_cvt_pk_f16_f32 v124, v38, v39
	v_cvt_pk_f16_f32 v125, v40, v41
	v_cvt_pk_f16_f32 v126, v34, v35
	v_cvt_pk_f16_f32 v127, v36, v37
	ds_write_b16 v118, v120
	ds_write_b16_d16_hi v118, v120 offset:528
	ds_write_b16 v118, v121 offset:1056
	ds_write_b16_d16_hi v118, v121 offset:1584
	ds_write_b16 v118, v122 offset:32
	ds_write_b16_d16_hi v118, v122 offset:560
	ds_write_b16 v118, v123 offset:1088
	ds_write_b16_d16_hi v118, v123 offset:1616
	ds_write_b16 v118, v124 offset:256
	ds_write_b16_d16_hi v118, v124 offset:784
	ds_write_b16 v118, v125 offset:1312
	ds_write_b16_d16_hi v118, v125 offset:1840
	ds_write_b16 v118, v126 offset:288
	ds_write_b16_d16_hi v118, v126 offset:816
	ds_write_b16 v118, v127 offset:1344
	ds_write_b16_d16_hi v118, v127 offset:1872
.Lmy_s5_end:
	s_add_i32 s54, s18, 112
	s_lshr_b32 s55, s54, 10
	v_pk_add_f32 v[30:31], v[204:205], v[30:31]
	v_pk_add_f32 v[32:33], v[206:207], v[32:33]
	v_pk_add_f32 v[26:27], v[204:205], v[26:27]
	v_pk_add_f32 v[28:29], v[206:207], v[28:29]
	v_pk_add_f32 v[22:23], v[204:205], v[22:23]
	v_pk_add_f32 v[24:25], v[206:207], v[24:25]
	v_pk_add_f32 v[18:19], v[204:205], v[18:19]
	v_pk_add_f32 v[20:21], v[206:207], v[20:21]
	s_cmp_eq_u32 s55, 2
	s_cbranch_scc1 .Lmy_s6_v
	v_add_u32_e32 v118, 0x9060, v113
	s_cmp_eq_u32 s55, 0
	s_cbranch_scc0 .Lmy_s6_ns
	v_pk_mul_f32 v[30:31], v[116:117], v[30:31]
	v_pk_mul_f32 v[32:33], v[116:117], v[32:33]
	v_pk_mul_f32 v[26:27], v[116:117], v[26:27]
	v_pk_mul_f32 v[28:29], v[116:117], v[28:29]
	v_pk_mul_f32 v[22:23], v[116:117], v[22:23]
	v_pk_mul_f32 v[24:25], v[116:117], v[24:25]
	v_pk_mul_f32 v[18:19], v[116:117], v[18:19]
	v_pk_mul_f32 v[20:21], v[116:117], v[20:21]

.Lmy_s6_v:
	v_add_u32_e32 v118, 0xf300, v114
	v_cvt_pk_f16_f32 v120, v30, v31
	v_cvt_pk_f16_f32 v121, v32, v33
	v_cvt_pk_f16_f32 v122, v26, v27
	v_cvt_pk_f16_f32 v123, v28, v29
	v_cvt_pk_f16_f32 v124, v22, v23
	v_cvt_pk_f16_f32 v125, v24, v25
	v_cvt_pk_f16_f32 v126, v18, v19
	v_cvt_pk_f16_f32 v127, v20, v21
	ds_write_b16 v118, v120
	ds_write_b16_d16_hi v118, v120 offset:528
	ds_write_b16 v118, v121 offset:1056
	ds_write_b16_d16_hi v118, v121 offset:1584
	ds_write_b16 v118, v122 offset:32
	ds_write_b16_d16_hi v118, v122 offset:560
	ds_write_b16 v118, v123 offset:1088
	ds_write_b16_d16_hi v118, v123 offset:1616
	ds_write_b16 v118, v124 offset:256
	ds_write_b16_d16_hi v118, v124 offset:784
	ds_write_b16 v118, v125 offset:1312
	ds_write_b16_d16_hi v118, v125 offset:1840
	ds_write_b16 v118, v126 offset:288
	ds_write_b16_d16_hi v118, v126 offset:816
	ds_write_b16 v118, v127 offset:1344
	ds_write_b16_d16_hi v118, v127 offset:1872

.Lmy_st1_wr1:
	s_add_i32 s54, s18, 64
	s_lshr_b32 s55, s54, 10
	v_pk_add_f32 v[78:79], v[192:193], v[78:79]
	v_pk_add_f32 v[80:81], v[194:195], v[80:81]
	v_pk_add_f32 v[74:75], v[192:193], v[74:75]
	v_pk_add_f32 v[76:77], v[194:195], v[76:77]
	v_pk_add_f32 v[70:71], v[192:193], v[70:71]
	v_pk_add_f32 v[72:73], v[194:195], v[72:73]
	v_pk_add_f32 v[66:67], v[192:193], v[66:67]
	v_pk_add_f32 v[68:69], v[194:195], v[68:69]
	s_cmp_eq_u32 s55, 2
	s_cbranch_scc1 .Lmy_s7_v
	v_add_u32_e32 v118, 0x9000, v113
	s_cmp_eq_u32 s55, 0
	s_cbranch_scc0 .Lmy_s7_ns
	v_pk_mul_f32 v[78:79], v[116:117], v[78:79]
	v_pk_mul_f32 v[80:81], v[116:117], v[80:81]
	v_pk_mul_f32 v[74:75], v[116:117], v[74:75]
	v_pk_mul_f32 v[76:77], v[116:117], v[76:77]
	v_pk_mul_f32 v[70:71], v[116:117], v[70:71]
	v_pk_mul_f32 v[72:73], v[116:117], v[72:73]
	v_pk_mul_f32 v[66:67], v[116:117], v[66:67]
	v_pk_mul_f32 v[68:69], v[116:117], v[68:69]

.Lmy_s7_v:
	v_add_u32_e32 v118, 0x9000, v114
	v_cvt_pk_f16_f32 v120, v78, v79
	v_cvt_pk_f16_f32 v121, v80, v81
	v_cvt_pk_f16_f32 v122, v74, v75
	v_cvt_pk_f16_f32 v123, v76, v77
	v_cvt_pk_f16_f32 v124, v70, v71
	v_cvt_pk_f16_f32 v125, v72, v73
	v_cvt_pk_f16_f32 v126, v66, v67
	v_cvt_pk_f16_f32 v127, v68, v69
	ds_write_b16 v118, v120
	ds_write_b16_d16_hi v118, v120 offset:528
	ds_write_b16 v118, v121 offset:1056
	ds_write_b16_d16_hi v118, v121 offset:1584
	ds_write_b16 v118, v122 offset:32
	ds_write_b16_d16_hi v118, v122 offset:560
	ds_write_b16 v118, v123 offset:1088
	ds_write_b16_d16_hi v118, v123 offset:1616
	ds_write_b16 v118, v124 offset:256
	ds_write_b16_d16_hi v118, v124 offset:784
	ds_write_b16 v118, v125 offset:1312
	ds_write_b16_d16_hi v118, v125 offset:1840
	ds_write_b16 v118, v126 offset:288
	ds_write_b16_d16_hi v118, v126 offset:816
	ds_write_b16 v118, v127 offset:1344
	ds_write_b16_d16_hi v118, v127 offset:1872
.Lmy_s7_end:
	s_add_i32 s54, s18, 80
	s_lshr_b32 s55, s54, 10
	v_pk_add_f32 v[62:63], v[196:197], v[62:63]
	v_pk_add_f32 v[64:65], v[198:199], v[64:65]
	v_pk_add_f32 v[58:59], v[196:197], v[58:59]
	v_pk_add_f32 v[60:61], v[198:199], v[60:61]
	v_pk_add_f32 v[54:55], v[196:197], v[54:55]
	v_pk_add_f32 v[56:57], v[198:199], v[56:57]
	v_pk_add_f32 v[50:51], v[196:197], v[50:51]
	v_pk_add_f32 v[52:53], v[198:199], v[52:53]
	s_cmp_eq_u32 s55, 2
	s_cbranch_scc1 .Lmy_s8_v
	v_add_u32_e32 v118, 0x9020, v113
	s_cmp_eq_u32 s55, 0
	s_cbranch_scc0 .Lmy_s8_ns
	v_pk_mul_f32 v[62:63], v[116:117], v[62:63]
	v_pk_mul_f32 v[64:65], v[116:117], v[64:65]
	v_pk_mul_f32 v[58:59], v[116:117], v[58:59]
	v_pk_mul_f32 v[60:61], v[116:117], v[60:61]
	v_pk_mul_f32 v[54:55], v[116:117], v[54:55]
	v_pk_mul_f32 v[56:57], v[116:117], v[56:57]
	v_pk_mul_f32 v[50:51], v[116:117], v[50:51]
	v_pk_mul_f32 v[52:53], v[116:117], v[52:53]

.Lmy_s8_v:
	v_add_u32_e32 v118, 0xb100, v114
	v_cvt_pk_f16_f32 v120, v62, v63
	v_cvt_pk_f16_f32 v121, v64, v65
	v_cvt_pk_f16_f32 v122, v58, v59
	v_cvt_pk_f16_f32 v123, v60, v61
	v_cvt_pk_f16_f32 v124, v54, v55
	v_cvt_pk_f16_f32 v125, v56, v57
	v_cvt_pk_f16_f32 v126, v50, v51
	v_cvt_pk_f16_f32 v127, v52, v53
	ds_write_b16 v118, v120
	ds_write_b16_d16_hi v118, v120 offset:528
	ds_write_b16 v118, v121 offset:1056
	ds_write_b16_d16_hi v118, v121 offset:1584
	ds_write_b16 v118, v122 offset:32
	ds_write_b16_d16_hi v118, v122 offset:560
	ds_write_b16 v118, v123 offset:1088
	ds_write_b16_d16_hi v118, v123 offset:1616
	ds_write_b16 v118, v124 offset:256
	ds_write_b16_d16_hi v118, v124 offset:784
	ds_write_b16 v118, v125 offset:1312
	ds_write_b16_d16_hi v118, v125 offset:1840
	ds_write_b16 v118, v126 offset:288
	ds_write_b16_d16_hi v118, v126 offset:816
	ds_write_b16 v118, v127 offset:1344
	ds_write_b16_d16_hi v118, v127 offset:1872
.Lmy_s8_end:
.Lmy_st1_done:
	s_waitcnt lgkmcnt(0)
	s_barrier
	s_add_i32 s54, s18, 64
	s_lshr_b32 s55, s54, 10
	s_bfe_u32 s56, s54, 0x40006
	s_lshr_b32 s57, s36, 3
	s_lshl_b32 s57, s57, 4
	s_add_i32 s57, s57, s56
	s_lshl_b32 s57, s57, 18
	s_and_b32 s58, s36, 7
	s_cmp_eq_u32 s55, 2
	s_cbranch_scc1 .Lmy_gs1_v
	s_lshl_b32 s58, s58, 15
	s_add_i32 s57, s57, s58
	s_cmp_eq_u32 s55, 0
	s_cselect_b32 s60, s6, s8
	s_cselect_b32 s61, s7, s9
	s_add_u32 s60, s60, s57
	s_addc_u32 s61, s61, 0
	v_add_u32_e32 v131, 0x9000, v128
	ds_read_b128 v[132:135], v131
	ds_read_b128 v[136:139], v131 offset:9216
	ds_read_b128 v[140:143], v131 offset:18432
	ds_read_b128 v[144:147], v131 offset:27648
	s_waitcnt lgkmcnt(3)
	global_store_dwordx4 v1, v[132:135], s[60:61] nt
	s_add_u32 s60, s60, 0x2000
	s_addc_u32 s61, s61, 0
	s_waitcnt lgkmcnt(2)
	global_store_dwordx4 v1, v[136:139], s[60:61] nt
	s_add_u32 s60, s60, 0x2000
	s_addc_u32 s61, s61, 0
	s_waitcnt lgkmcnt(1)
	global_store_dwordx4 v1, v[140:143], s[60:61] nt
	s_add_u32 s60, s60, 0x2000
	s_addc_u32 s61, s61, 0
	s_waitcnt lgkmcnt(0)
	global_store_dwordx4 v1, v[144:147], s[60:61] nt
	s_branch .Lmy_gs1_end
.Lmy_gs1_v:
	s_lshl_b32 s58, s58, 9
	s_add_i32 s57, s57, s58
	s_add_u32 s60, s10, s57
	s_addc_u32 s61, s11, 0
	v_add_u32_e32 v131, 0x9000, v129
	ds_read_b128 v[132:135], v131
	ds_read_b128 v[136:139], v131 offset:8448
	ds_read_b128 v[140:143], v131 offset:16896
	ds_read_b128 v[144:147], v131 offset:25344
	s_waitcnt lgkmcnt(3)
	global_store_dwordx4 v130, v[132:135], s[60:61] nt
	s_add_u32 s60, s60, 0x10000
	s_addc_u32 s61, s61, 0
	s_waitcnt lgkmcnt(2)
	global_store_dwordx4 v130, v[136:139], s[60:61] nt
	s_add_u32 s60, s60, 0x10000
	s_addc_u32 s61, s61, 0
	s_waitcnt lgkmcnt(1)
	global_store_dwordx4 v130, v[140:143], s[60:61] nt
	s_add_u32 s60, s60, 0x10000
	s_addc_u32 s61, s61, 0
	s_waitcnt lgkmcnt(0)
	global_store_dwordx4 v130, v[144:147], s[60:61] nt
.Lmy_gs1_end:
	s_cmp_lg_u32 s37, 0
	s_cbranch_scc1 .Lmy_st2_wr1
	s_add_i32 s54, s18, 128
	s_lshr_b32 s55, s54, 10
	v_pk_add_f32 v[14:15], v[208:209], v[14:15]
	v_pk_add_f32 v[16:17], v[210:211], v[16:17]
	v_pk_add_f32 v[10:11], v[208:209], v[10:11]
	v_pk_add_f32 v[12:13], v[210:211], v[12:13]
	v_pk_add_f32 v[6:7], v[208:209], v[6:7]
	v_pk_add_f32 v[8:9], v[210:211], v[8:9]
	v_pk_add_f32 v[2:3], v[208:209], v[2:3]
	v_pk_add_f32 v[4:5], v[210:211], v[4:5]
	s_cmp_eq_u32 s55, 2
	s_cbranch_scc1 .Lmy_s9_v
	v_add_u32_e32 v118, 0x12000, v113
	s_cmp_eq_u32 s55, 0
	s_cbranch_scc0 .Lmy_s9_ns
	v_pk_mul_f32 v[14:15], v[116:117], v[14:15]
	v_pk_mul_f32 v[16:17], v[116:117], v[16:17]
	v_pk_mul_f32 v[10:11], v[116:117], v[10:11]
	v_pk_mul_f32 v[12:13], v[116:117], v[12:13]
	v_pk_mul_f32 v[6:7], v[116:117], v[6:7]
	v_pk_mul_f32 v[8:9], v[116:117], v[8:9]
	v_pk_mul_f32 v[2:3], v[116:117], v[2:3]
	v_pk_mul_f32 v[4:5], v[116:117], v[4:5]

.Lmy_s9_v:
	v_add_u32_e32 v118, 0x12000, v114
	v_cvt_pk_f16_f32 v120, v14, v15
	v_cvt_pk_f16_f32 v121, v16, v17
	v_cvt_pk_f16_f32 v122, v10, v11
	v_cvt_pk_f16_f32 v123, v12, v13
	v_cvt_pk_f16_f32 v124, v6, v7
	v_cvt_pk_f16_f32 v125, v8, v9
	v_cvt_pk_f16_f32 v126, v2, v3
	v_cvt_pk_f16_f32 v127, v4, v5
	ds_write_b16 v118, v120
	ds_write_b16_d16_hi v118, v120 offset:528
	ds_write_b16 v118, v121 offset:1056
	ds_write_b16_d16_hi v118, v121 offset:1584
	ds_write_b16 v118, v122 offset:32
	ds_write_b16_d16_hi v118, v122 offset:560
	ds_write_b16 v118, v123 offset:1088
	ds_write_b16_d16_hi v118, v123 offset:1616
	ds_write_b16 v118, v124 offset:256
	ds_write_b16_d16_hi v118, v124 offset:784
	ds_write_b16 v118, v125 offset:1312
	ds_write_b16_d16_hi v118, v125 offset:1840
	ds_write_b16 v118, v126 offset:288
	ds_write_b16_d16_hi v118, v126 offset:816
	ds_write_b16 v118, v127 offset:1344
	ds_write_b16_d16_hi v118, v127 offset:1872

.Lmy_st2_wr1:
	s_add_i32 s54, s18, 144
	s_lshr_b32 s55, s54, 10
	v_pk_add_f32 v[46:47], v[200:201], v[46:47]
	v_pk_add_f32 v[48:49], v[202:203], v[48:49]
	v_pk_add_f32 v[42:43], v[200:201], v[42:43]
	v_pk_add_f32 v[44:45], v[202:203], v[44:45]
	v_pk_add_f32 v[38:39], v[200:201], v[38:39]
	v_pk_add_f32 v[40:41], v[202:203], v[40:41]
	v_pk_add_f32 v[34:35], v[200:201], v[34:35]
	v_pk_add_f32 v[36:37], v[202:203], v[36:37]
	s_cmp_eq_u32 s55, 2
	s_cbranch_scc1 .Lmy_s10_v
	v_add_u32_e32 v118, 0x12020, v113
	s_cmp_eq_u32 s55, 0
	s_cbranch_scc0 .Lmy_s10_ns
	v_pk_mul_f32 v[46:47], v[116:117], v[46:47]
	v_pk_mul_f32 v[48:49], v[116:117], v[48:49]
	v_pk_mul_f32 v[42:43], v[116:117], v[42:43]
	v_pk_mul_f32 v[44:45], v[116:117], v[44:45]
	v_pk_mul_f32 v[38:39], v[116:117], v[38:39]
	v_pk_mul_f32 v[40:41], v[116:117], v[40:41]
	v_pk_mul_f32 v[34:35], v[116:117], v[34:35]
	v_pk_mul_f32 v[36:37], v[116:117], v[36:37]

.Lmy_s10_v:
	v_add_u32_e32 v118, 0x14100, v114
	v_cvt_pk_f16_f32 v120, v46, v47
	v_cvt_pk_f16_f32 v121, v48, v49
	v_cvt_pk_f16_f32 v122, v42, v43
	v_cvt_pk_f16_f32 v123, v44, v45
	v_cvt_pk_f16_f32 v124, v38, v39
	v_cvt_pk_f16_f32 v125, v40, v41
	v_cvt_pk_f16_f32 v126, v34, v35
	v_cvt_pk_f16_f32 v127, v36, v37
	ds_write_b16 v118, v120
	ds_write_b16_d16_hi v118, v120 offset:528
	ds_write_b16 v118, v121 offset:1056
	ds_write_b16_d16_hi v118, v121 offset:1584
	ds_write_b16 v118, v122 offset:32
	ds_write_b16_d16_hi v118, v122 offset:560
	ds_write_b16 v118, v123 offset:1088
	ds_write_b16_d16_hi v118, v123 offset:1616
	ds_write_b16 v118, v124 offset:256
	ds_write_b16_d16_hi v118, v124 offset:784
	ds_write_b16 v118, v125 offset:1312
	ds_write_b16_d16_hi v118, v125 offset:1840
	ds_write_b16 v118, v126 offset:288
	ds_write_b16_d16_hi v118, v126 offset:816
	ds_write_b16 v118, v127 offset:1344
	ds_write_b16_d16_hi v118, v127 offset:1872
.Lmy_s10_end:
	s_add_i32 s54, s18, 160
	s_lshr_b32 s55, s54, 10
	v_pk_add_f32 v[30:31], v[204:205], v[30:31]
	v_pk_add_f32 v[32:33], v[206:207], v[32:33]
	v_pk_add_f32 v[26:27], v[204:205], v[26:27]
	v_pk_add_f32 v[28:29], v[206:207], v[28:29]
	v_pk_add_f32 v[22:23], v[204:205], v[22:23]
	v_pk_add_f32 v[24:25], v[206:207], v[24:25]
	v_pk_add_f32 v[18:19], v[204:205], v[18:19]
	v_pk_add_f32 v[20:21], v[206:207], v[20:21]
	s_cmp_eq_u32 s55, 2
	s_cbranch_scc1 .Lmy_s11_v
	v_add_u32_e32 v118, 0x12040, v113
	s_cmp_eq_u32 s55, 0
	s_cbranch_scc0 .Lmy_s11_ns
	v_pk_mul_f32 v[30:31], v[116:117], v[30:31]
	v_pk_mul_f32 v[32:33], v[116:117], v[32:33]
	v_pk_mul_f32 v[26:27], v[116:117], v[26:27]
	v_pk_mul_f32 v[28:29], v[116:117], v[28:29]
	v_pk_mul_f32 v[22:23], v[116:117], v[22:23]
	v_pk_mul_f32 v[24:25], v[116:117], v[24:25]
	v_pk_mul_f32 v[18:19], v[116:117], v[18:19]
	v_pk_mul_f32 v[20:21], v[116:117], v[20:21]

.Lmy_s11_v:
	v_add_u32_e32 v118, 0x16200, v114
	v_cvt_pk_f16_f32 v120, v30, v31
	v_cvt_pk_f16_f32 v121, v32, v33
	v_cvt_pk_f16_f32 v122, v26, v27
	v_cvt_pk_f16_f32 v123, v28, v29
	v_cvt_pk_f16_f32 v124, v22, v23
	v_cvt_pk_f16_f32 v125, v24, v25
	v_cvt_pk_f16_f32 v126, v18, v19
	v_cvt_pk_f16_f32 v127, v20, v21
	ds_write_b16 v118, v120
	ds_write_b16_d16_hi v118, v120 offset:528
	ds_write_b16 v118, v121 offset:1056
	ds_write_b16_d16_hi v118, v121 offset:1584
	ds_write_b16 v118, v122 offset:32
	ds_write_b16_d16_hi v118, v122 offset:560
	ds_write_b16 v118, v123 offset:1088
	ds_write_b16_d16_hi v118, v123 offset:1616
	ds_write_b16 v118, v124 offset:256
	ds_write_b16_d16_hi v118, v124 offset:784
	ds_write_b16 v118, v125 offset:1312
	ds_write_b16_d16_hi v118, v125 offset:1840
	ds_write_b16 v118, v126 offset:288
	ds_write_b16_d16_hi v118, v126 offset:816
	ds_write_b16 v118, v127 offset:1344
	ds_write_b16_d16_hi v118, v127 offset:1872
.Lmy_s11_end:
	s_add_i32 s54, s18, 176
	s_lshr_b32 s55, s54, 10
	v_pk_add_f32 v[14:15], v[208:209], v[14:15]
	v_pk_add_f32 v[16:17], v[210:211], v[16:17]
	v_pk_add_f32 v[10:11], v[208:209], v[10:11]
	v_pk_add_f32 v[12:13], v[210:211], v[12:13]
	v_pk_add_f32 v[6:7], v[208:209], v[6:7]
	v_pk_add_f32 v[8:9], v[210:211], v[8:9]
	v_pk_add_f32 v[2:3], v[208:209], v[2:3]
	v_pk_add_f32 v[4:5], v[210:211], v[4:5]
	s_cmp_eq_u32 s55, 2
	s_cbranch_scc1 .Lmy_s12_v
	v_add_u32_e32 v118, 0x12060, v113
	s_cmp_eq_u32 s55, 0
	s_cbranch_scc0 .Lmy_s12_ns
	v_pk_mul_f32 v[14:15], v[116:117], v[14:15]
	v_pk_mul_f32 v[16:17], v[116:117], v[16:17]
	v_pk_mul_f32 v[10:11], v[116:117], v[10:11]
	v_pk_mul_f32 v[12:13], v[116:117], v[12:13]
	v_pk_mul_f32 v[6:7], v[116:117], v[6:7]
	v_pk_mul_f32 v[8:9], v[116:117], v[8:9]
	v_pk_mul_f32 v[2:3], v[116:117], v[2:3]
	v_pk_mul_f32 v[4:5], v[116:117], v[4:5]

.Lmy_s12_v:
	v_add_u32_e32 v118, 0x18300, v114
	v_cvt_pk_f16_f32 v120, v14, v15
	v_cvt_pk_f16_f32 v121, v16, v17
	v_cvt_pk_f16_f32 v122, v10, v11
	v_cvt_pk_f16_f32 v123, v12, v13
	v_cvt_pk_f16_f32 v124, v6, v7
	v_cvt_pk_f16_f32 v125, v8, v9
	v_cvt_pk_f16_f32 v126, v2, v3
	v_cvt_pk_f16_f32 v127, v4, v5
	ds_write_b16 v118, v120
	ds_write_b16_d16_hi v118, v120 offset:528
	ds_write_b16 v118, v121 offset:1056
	ds_write_b16_d16_hi v118, v121 offset:1584
	ds_write_b16 v118, v122 offset:32
	ds_write_b16_d16_hi v118, v122 offset:560
	ds_write_b16 v118, v123 offset:1088
	ds_write_b16_d16_hi v118, v123 offset:1616
	ds_write_b16 v118, v124 offset:256
	ds_write_b16_d16_hi v118, v124 offset:784
	ds_write_b16 v118, v125 offset:1312
	ds_write_b16_d16_hi v118, v125 offset:1840
	ds_write_b16 v118, v126 offset:288
	ds_write_b16_d16_hi v118, v126 offset:816
	ds_write_b16 v118, v127 offset:1344
	ds_write_b16_d16_hi v118, v127 offset:1872
.Lmy_s12_end:
.Lmy_st2_done:
	s_waitcnt lgkmcnt(0)
	s_barrier
	s_add_i32 s54, s18, 128
	s_lshr_b32 s55, s54, 10
	s_bfe_u32 s56, s54, 0x40006
	s_lshr_b32 s57, s36, 3
	s_lshl_b32 s57, s57, 4
	s_add_i32 s57, s57, s56
	s_lshl_b32 s57, s57, 18
	s_and_b32 s58, s36, 7
	s_cmp_eq_u32 s55, 2
	s_cbranch_scc1 .Lmy_gs2_v
	s_lshl_b32 s58, s58, 15
	s_add_i32 s57, s57, s58
	s_cmp_eq_u32 s55, 0
	s_cselect_b32 s60, s6, s8
	s_cselect_b32 s61, s7, s9
	s_add_u32 s60, s60, s57
	s_addc_u32 s61, s61, 0
	v_add_u32_e32 v131, 0x12000, v128
	ds_read_b128 v[132:135], v131
	ds_read_b128 v[136:139], v131 offset:9216
	ds_read_b128 v[140:143], v131 offset:18432
	ds_read_b128 v[144:147], v131 offset:27648
	s_waitcnt lgkmcnt(3)
	global_store_dwordx4 v1, v[132:135], s[60:61] nt
	s_add_u32 s60, s60, 0x2000
	s_addc_u32 s61, s61, 0
	s_waitcnt lgkmcnt(2)
	global_store_dwordx4 v1, v[136:139], s[60:61] nt
	s_add_u32 s60, s60, 0x2000
	s_addc_u32 s61, s61, 0
	s_waitcnt lgkmcnt(1)
	global_store_dwordx4 v1, v[140:143], s[60:61] nt
	s_add_u32 s60, s60, 0x2000
	s_addc_u32 s61, s61, 0
	s_waitcnt lgkmcnt(0)
	global_store_dwordx4 v1, v[144:147], s[60:61] nt
	s_branch .Lmy_gs2_end
.Lmy_gs2_v:
	s_lshl_b32 s58, s58, 9
	s_add_i32 s57, s57, s58
	s_add_u32 s60, s10, s57
	s_addc_u32 s61, s11, 0
	v_add_u32_e32 v131, 0x12000, v129
	ds_read_b128 v[132:135], v131
	ds_read_b128 v[136:139], v131 offset:8448
	ds_read_b128 v[140:143], v131 offset:16896
	ds_read_b128 v[144:147], v131 offset:25344
	s_waitcnt lgkmcnt(3)
	global_store_dwordx4 v130, v[132:135], s[60:61] nt
	s_add_u32 s60, s60, 0x10000
	s_addc_u32 s61, s61, 0
	s_waitcnt lgkmcnt(2)
	global_store_dwordx4 v130, v[136:139], s[60:61] nt
	s_add_u32 s60, s60, 0x10000
	s_addc_u32 s61, s61, 0
	s_waitcnt lgkmcnt(1)
	global_store_dwordx4 v130, v[140:143], s[60:61] nt
	s_add_u32 s60, s60, 0x10000
	s_addc_u32 s61, s61, 0
	s_waitcnt lgkmcnt(0)
	global_store_dwordx4 v130, v[144:147], s[60:61] nt
